# code placement: .p2align 6 in front of the nine GEMM K-loop heads and the two attention loop heads (attention main loop had moved from 0 to 4 mod 8 bytes since the baseline); on top of v62
# speedup vs baseline: 1.0007x; 1.0001x over previous
.LBB0_298:
	s_ashr_i32 s15, s14, 31
	s_lshl_b64 s[16:17], s[14:15], 19
	s_add_u32 s16, s2, s16
	s_addc_u32 s17, s3, s17
	s_and_b64 s[18:19], s[4:5], exec
	s_cselect_b32 s15, s17, s23
	s_cselect_b32 s48, s16, s22
	s_ashr_i32 s13, s12, 31
	s_lshl_b64 s[18:19], s[12:13], 19
	s_add_u32 s18, s28, s18
	s_addc_u32 s19, s29, s19
	s_and_b64 s[26:27], s[4:5], exec
	s_cselect_b32 s13, s19, s25
	s_cselect_b32 s49, s18, s24
	s_add_u32 s22, s22, 0x40080
	s_addc_u32 s23, s23, 0
	s_add_u32 s50, s24, 0x100
	v_mov_b32_e32 v2, 0
	s_addc_u32 s51, s25, 0
	s_mov_b32 s52, -2
	v_mov_b32_e32 v3, v2
	v_mov_b32_e32 v4, v2
	v_mov_b32_e32 v5, v2
	v_mov_b32_e32 v6, v2
	v_mov_b32_e32 v7, v2
	v_mov_b32_e32 v8, v2
	v_mov_b32_e32 v9, v2
	v_mov_b32_e32 v14, v2
	v_mov_b32_e32 v15, v2
	v_mov_b32_e32 v16, v2
	v_mov_b32_e32 v17, v2
	v_mov_b32_e32 v22, v2
	v_mov_b32_e32 v23, v2
	v_mov_b32_e32 v24, v2
	v_mov_b32_e32 v25, v2
	v_mov_b32_e32 v30, v2
	v_mov_b32_e32 v31, v2
	v_mov_b32_e32 v32, v2
	v_mov_b32_e32 v33, v2
	v_mov_b32_e32 v38, v2
	v_mov_b32_e32 v39, v2
	v_mov_b32_e32 v40, v2
	v_mov_b32_e32 v41, v2
	v_mov_b32_e32 v46, v2
	v_mov_b32_e32 v47, v2
	v_mov_b32_e32 v48, v2
	v_mov_b32_e32 v49, v2
	v_mov_b32_e32 v54, v2
	v_mov_b32_e32 v55, v2
	v_mov_b32_e32 v56, v2
	v_mov_b32_e32 v57, v2
	v_mov_b32_e32 v10, v2
	v_mov_b32_e32 v11, v2
	v_mov_b32_e32 v12, v2
	v_mov_b32_e32 v13, v2
	v_mov_b32_e32 v18, v2
	v_mov_b32_e32 v19, v2
	v_mov_b32_e32 v20, v2
	v_mov_b32_e32 v21, v2
	v_mov_b32_e32 v26, v2
	v_mov_b32_e32 v27, v2
	v_mov_b32_e32 v28, v2
	v_mov_b32_e32 v29, v2
	v_mov_b32_e32 v34, v2
	v_mov_b32_e32 v35, v2
	v_mov_b32_e32 v36, v2
	v_mov_b32_e32 v37, v2
	v_mov_b32_e32 v42, v2
	v_mov_b32_e32 v43, v2
	v_mov_b32_e32 v44, v2
	v_mov_b32_e32 v45, v2
	v_mov_b32_e32 v50, v2
	v_mov_b32_e32 v51, v2
	v_mov_b32_e32 v52, v2
	v_mov_b32_e32 v53, v2
	v_mov_b32_e32 v58, v2
	v_mov_b32_e32 v59, v2
	v_mov_b32_e32 v60, v2
	v_mov_b32_e32 v61, v2
	v_mov_b32_e32 v62, v2
	v_mov_b32_e32 v63, v2
	v_mov_b32_e32 v64, v2
	v_mov_b32_e32 v65, v2
	v_mov_b32_e32 v66, v2
	v_mov_b32_e32 v67, v2
	v_mov_b32_e32 v68, v2
	v_mov_b32_e32 v69, v2
	v_mov_b32_e32 v70, v2
	v_mov_b32_e32 v71, v2
	v_mov_b32_e32 v72, v2
	v_mov_b32_e32 v73, v2
	v_mov_b32_e32 v78, v2
	v_mov_b32_e32 v79, v2
	v_mov_b32_e32 v80, v2
	v_mov_b32_e32 v81, v2
	v_mov_b32_e32 v86, v2
	v_mov_b32_e32 v87, v2
	v_mov_b32_e32 v88, v2
	v_mov_b32_e32 v89, v2
	v_mov_b32_e32 v94, v2
	v_mov_b32_e32 v95, v2
	v_mov_b32_e32 v96, v2
	v_mov_b32_e32 v97, v2
	v_mov_b32_e32 v102, v2
	v_mov_b32_e32 v103, v2
	v_mov_b32_e32 v104, v2
	v_mov_b32_e32 v105, v2
	v_mov_b32_e32 v110, v2
	v_mov_b32_e32 v111, v2
	v_mov_b32_e32 v112, v2
	v_mov_b32_e32 v113, v2
	v_mov_b32_e32 v118, v2
	v_mov_b32_e32 v119, v2
	v_mov_b32_e32 v120, v2
	v_mov_b32_e32 v121, v2
	v_mov_b32_e32 v74, v2
	v_mov_b32_e32 v75, v2
	v_mov_b32_e32 v76, v2
	v_mov_b32_e32 v77, v2
	v_mov_b32_e32 v82, v2
	v_mov_b32_e32 v83, v2
	v_mov_b32_e32 v84, v2
	v_mov_b32_e32 v85, v2
	v_mov_b32_e32 v90, v2
	v_mov_b32_e32 v91, v2
	v_mov_b32_e32 v92, v2
	v_mov_b32_e32 v93, v2
	v_mov_b32_e32 v98, v2
	v_mov_b32_e32 v99, v2
	v_mov_b32_e32 v100, v2
	v_mov_b32_e32 v101, v2
	v_mov_b32_e32 v106, v2
	v_mov_b32_e32 v107, v2
	v_mov_b32_e32 v108, v2
	v_mov_b32_e32 v109, v2
	v_mov_b32_e32 v114, v2
	v_mov_b32_e32 v115, v2
	v_mov_b32_e32 v116, v2
	v_mov_b32_e32 v117, v2
	v_mov_b32_e32 v122, v2
	v_mov_b32_e32 v123, v2
	v_mov_b32_e32 v124, v2
	v_mov_b32_e32 v125, v2
	v_mov_b32_e32 v126, v2
	v_mov_b32_e32 v127, v2
	v_mov_b32_e32 v128, v2
	v_mov_b32_e32 v129, v2
	.p2align 6

.LBB0_835:
	s_ashr_i32 s15, s14, 31
	s_lshl_b64 s[16:17], s[14:15], 19
	s_add_u32 s16, s2, s16
	s_addc_u32 s17, s3, s17
	s_and_b64 s[18:19], s[4:5], exec
	s_cselect_b32 s15, s17, s23
	s_cselect_b32 s42, s16, s22
	s_ashr_i32 s13, s12, 31
	s_lshl_b64 s[18:19], s[12:13], 19
	v_readlane_b32 s26, v253, 38
	v_readlane_b32 s27, v253, 39
	s_add_u32 s18, s26, s18
	s_addc_u32 s19, s27, s19
	s_and_b64 s[26:27], s[4:5], exec
	s_cselect_b32 s13, s19, s25
	s_cselect_b32 s43, s18, s24
	s_add_u32 s22, s22, 0x40080
	s_addc_u32 s23, s23, 0
	s_add_u32 s44, s24, 0x100
	v_mov_b32_e32 v2, 0
	s_addc_u32 s45, s25, 0
	s_mov_b32 s46, -2
	v_mov_b32_e32 v3, v2
	v_mov_b32_e32 v4, v2
	v_mov_b32_e32 v5, v2
	v_mov_b32_e32 v6, v2
	v_mov_b32_e32 v7, v2
	v_mov_b32_e32 v8, v2
	v_mov_b32_e32 v9, v2
	v_mov_b32_e32 v10, v2
	v_mov_b32_e32 v11, v2
	v_mov_b32_e32 v12, v2
	v_mov_b32_e32 v13, v2
	v_mov_b32_e32 v14, v2
	v_mov_b32_e32 v15, v2
	v_mov_b32_e32 v16, v2
	v_mov_b32_e32 v17, v2
	v_mov_b32_e32 v34, v2
	v_mov_b32_e32 v35, v2
	v_mov_b32_e32 v36, v2
	v_mov_b32_e32 v37, v2
	v_mov_b32_e32 v38, v2
	v_mov_b32_e32 v39, v2
	v_mov_b32_e32 v40, v2
	v_mov_b32_e32 v41, v2
	v_mov_b32_e32 v42, v2
	v_mov_b32_e32 v43, v2
	v_mov_b32_e32 v44, v2
	v_mov_b32_e32 v45, v2
	v_mov_b32_e32 v46, v2
	v_mov_b32_e32 v47, v2
	v_mov_b32_e32 v48, v2
	v_mov_b32_e32 v49, v2
	v_mov_b32_e32 v18, v2
	v_mov_b32_e32 v19, v2
	v_mov_b32_e32 v20, v2
	v_mov_b32_e32 v21, v2
	v_mov_b32_e32 v22, v2
	v_mov_b32_e32 v23, v2
	v_mov_b32_e32 v24, v2
	v_mov_b32_e32 v25, v2
	v_mov_b32_e32 v26, v2
	v_mov_b32_e32 v27, v2
	v_mov_b32_e32 v28, v2
	v_mov_b32_e32 v29, v2
	v_mov_b32_e32 v30, v2
	v_mov_b32_e32 v31, v2
	v_mov_b32_e32 v32, v2
	v_mov_b32_e32 v33, v2
	v_mov_b32_e32 v50, v2
	v_mov_b32_e32 v51, v2
	v_mov_b32_e32 v52, v2
	v_mov_b32_e32 v53, v2
	v_mov_b32_e32 v54, v2
	v_mov_b32_e32 v55, v2
	v_mov_b32_e32 v56, v2
	v_mov_b32_e32 v57, v2
	v_mov_b32_e32 v58, v2
	v_mov_b32_e32 v59, v2
	v_mov_b32_e32 v60, v2
	v_mov_b32_e32 v61, v2
	v_mov_b32_e32 v62, v2
	v_mov_b32_e32 v63, v2
	v_mov_b32_e32 v64, v2
	v_mov_b32_e32 v65, v2
	v_mov_b32_e32 v66, v2
	v_mov_b32_e32 v67, v2
	v_mov_b32_e32 v68, v2
	v_mov_b32_e32 v69, v2
	v_mov_b32_e32 v70, v2
	v_mov_b32_e32 v71, v2
	v_mov_b32_e32 v72, v2
	v_mov_b32_e32 v73, v2
	v_mov_b32_e32 v74, v2
	v_mov_b32_e32 v75, v2
	v_mov_b32_e32 v76, v2
	v_mov_b32_e32 v77, v2
	v_mov_b32_e32 v78, v2
	v_mov_b32_e32 v79, v2
	v_mov_b32_e32 v80, v2
	v_mov_b32_e32 v81, v2
	v_mov_b32_e32 v98, v2
	v_mov_b32_e32 v99, v2
	v_mov_b32_e32 v100, v2
	v_mov_b32_e32 v101, v2
	v_mov_b32_e32 v102, v2
	v_mov_b32_e32 v103, v2
	v_mov_b32_e32 v104, v2
	v_mov_b32_e32 v105, v2
	v_mov_b32_e32 v106, v2
	v_mov_b32_e32 v107, v2
	v_mov_b32_e32 v108, v2
	v_mov_b32_e32 v109, v2
	v_mov_b32_e32 v110, v2
	v_mov_b32_e32 v111, v2
	v_mov_b32_e32 v112, v2
	v_mov_b32_e32 v113, v2
	v_mov_b32_e32 v82, v2
	v_mov_b32_e32 v83, v2
	v_mov_b32_e32 v84, v2
	v_mov_b32_e32 v85, v2
	v_mov_b32_e32 v86, v2
	v_mov_b32_e32 v87, v2
	v_mov_b32_e32 v88, v2
	v_mov_b32_e32 v89, v2
	v_mov_b32_e32 v90, v2
	v_mov_b32_e32 v91, v2
	v_mov_b32_e32 v92, v2
	v_mov_b32_e32 v93, v2
	v_mov_b32_e32 v94, v2
	v_mov_b32_e32 v95, v2
	v_mov_b32_e32 v96, v2
	v_mov_b32_e32 v97, v2
	v_mov_b32_e32 v114, v2
	v_mov_b32_e32 v115, v2
	v_mov_b32_e32 v116, v2
	v_mov_b32_e32 v117, v2
	v_mov_b32_e32 v118, v2
	v_mov_b32_e32 v119, v2
	v_mov_b32_e32 v120, v2
	v_mov_b32_e32 v121, v2
	v_mov_b32_e32 v122, v2
	v_mov_b32_e32 v123, v2
	v_mov_b32_e32 v124, v2
	v_mov_b32_e32 v125, v2
	v_mov_b32_e32 v126, v2
	v_mov_b32_e32 v127, v2
	v_mov_b32_e32 v128, v2
	v_mov_b32_e32 v129, v2
	.p2align 6

.LBB0_1021:
	s_and_b64 s[0:1], s[18:19], exec
	s_cselect_b32 s57, s51, s56
	s_cmpk_gt_i32 s54, 0x80
	s_cselect_b64 s[18:19], -1, 0
	s_add_u32 s58, s20, 0x100
	v_lshl_add_u32 v138, s56, 2, v153
	s_addc_u32 s59, s21, 0
	s_mov_b64 s[22:23], -1
	s_and_b64 vcc, exec, s[18:19]
	s_cbranch_vccnz .LBB0_1025
	s_add_u32 s0, s20, 0x100
	v_mov_b32_e32 v34, 0
	s_addc_u32 s1, s21, 0
	s_mov_b32 s60, -2
	s_mov_b64 s[20:21], s[12:13]
	v_mov_b32_e32 v35, v34
	v_mov_b32_e32 v36, v34
	v_mov_b32_e32 v37, v34
	v_mov_b32_e32 v38, v34
	v_mov_b32_e32 v39, v34
	v_mov_b32_e32 v40, v34
	v_mov_b32_e32 v41, v34
	v_mov_b32_e32 v66, v34
	v_mov_b32_e32 v67, v34
	v_mov_b32_e32 v68, v34
	v_mov_b32_e32 v69, v34
	v_mov_b32_e32 v74, v34
	v_mov_b32_e32 v75, v34
	v_mov_b32_e32 v76, v34
	v_mov_b32_e32 v77, v34
	v_mov_b32_e32 v98, v34
	v_mov_b32_e32 v99, v34
	v_mov_b32_e32 v100, v34
	v_mov_b32_e32 v101, v34
	v_mov_b32_e32 v102, v34
	v_mov_b32_e32 v103, v34
	v_mov_b32_e32 v104, v34
	v_mov_b32_e32 v105, v34
	v_mov_b32_e32 v114, v34
	v_mov_b32_e32 v115, v34
	v_mov_b32_e32 v116, v34
	v_mov_b32_e32 v117, v34
	v_mov_b32_e32 v118, v34
	v_mov_b32_e32 v119, v34
	v_mov_b32_e32 v120, v34
	v_mov_b32_e32 v121, v34
	v_mov_b32_e32 v46, v34
	v_mov_b32_e32 v47, v34
	v_mov_b32_e32 v48, v34
	v_mov_b32_e32 v49, v34
	v_mov_b32_e32 v62, v34
	v_mov_b32_e32 v63, v34
	v_mov_b32_e32 v64, v34
	v_mov_b32_e32 v65, v34
	v_mov_b32_e32 v82, v34
	v_mov_b32_e32 v83, v34
	v_mov_b32_e32 v84, v34
	v_mov_b32_e32 v85, v34
	v_mov_b32_e32 v94, v34
	v_mov_b32_e32 v95, v34
	v_mov_b32_e32 v96, v34
	v_mov_b32_e32 v97, v34
	v_mov_b32_e32 v106, v34
	v_mov_b32_e32 v107, v34
	v_mov_b32_e32 v108, v34
	v_mov_b32_e32 v109, v34
	v_mov_b32_e32 v110, v34
	v_mov_b32_e32 v111, v34
	v_mov_b32_e32 v112, v34
	v_mov_b32_e32 v113, v34
	v_mov_b32_e32 v122, v34
	v_mov_b32_e32 v123, v34
	v_mov_b32_e32 v124, v34
	v_mov_b32_e32 v125, v34
	v_mov_b32_e32 v126, v34
	v_mov_b32_e32 v127, v34
	v_mov_b32_e32 v128, v34
	v_mov_b32_e32 v129, v34
	.p2align 6

.LBB0_1025:
	v_mov_b32_e32 v93, 0
	s_and_b64 vcc, exec, s[22:23]
	v_mov_b32_e32 v92, v93
	v_mov_b32_e32 v91, v93
	v_mov_b32_e32 v90, v93
	v_mov_b32_e32 v81, v93
	v_mov_b32_e32 v80, v93
	v_mov_b32_e32 v79, v93
	v_mov_b32_e32 v78, v93
	v_mov_b32_e32 v61, v93
	v_mov_b32_e32 v60, v93
	v_mov_b32_e32 v59, v93
	v_mov_b32_e32 v58, v93
	v_mov_b32_e32 v53, v93
	v_mov_b32_e32 v52, v93
	v_mov_b32_e32 v51, v93
	v_mov_b32_e32 v50, v93
	v_mov_b32_e32 v33, v93
	v_mov_b32_e32 v32, v93
	v_mov_b32_e32 v31, v93
	v_mov_b32_e32 v30, v93
	v_mov_b32_e32 v25, v93
	v_mov_b32_e32 v24, v93
	v_mov_b32_e32 v23, v93
	v_mov_b32_e32 v22, v93
	v_mov_b32_e32 v17, v93
	v_mov_b32_e32 v16, v93
	v_mov_b32_e32 v15, v93
	v_mov_b32_e32 v14, v93
	v_mov_b32_e32 v9, v93
	v_mov_b32_e32 v8, v93
	v_mov_b32_e32 v7, v93
	v_mov_b32_e32 v6, v93
	v_mov_b32_e32 v89, v93
	v_mov_b32_e32 v88, v93
	v_mov_b32_e32 v87, v93
	v_mov_b32_e32 v86, v93
	v_mov_b32_e32 v73, v93
	v_mov_b32_e32 v72, v93
	v_mov_b32_e32 v71, v93
	v_mov_b32_e32 v70, v93
	v_mov_b32_e32 v57, v93
	v_mov_b32_e32 v56, v93
	v_mov_b32_e32 v55, v93
	v_mov_b32_e32 v54, v93
	v_mov_b32_e32 v45, v93
	v_mov_b32_e32 v44, v93
	v_mov_b32_e32 v43, v93
	v_mov_b32_e32 v42, v93
	v_mov_b32_e32 v29, v93
	v_mov_b32_e32 v28, v93
	v_mov_b32_e32 v27, v93
	v_mov_b32_e32 v26, v93
	v_mov_b32_e32 v21, v93
	v_mov_b32_e32 v20, v93
	v_mov_b32_e32 v19, v93
	v_mov_b32_e32 v18, v93
	v_mov_b32_e32 v13, v93
	v_mov_b32_e32 v12, v93
	v_mov_b32_e32 v11, v93
	v_mov_b32_e32 v10, v93
	v_mov_b32_e32 v5, v93
	v_mov_b32_e32 v4, v93
	v_mov_b32_e32 v3, v93
	v_mov_b32_e32 v2, v93
	s_cbranch_vccz .LBB0_1029
	v_mov_b32_e32 v2, 0
	s_mov_b32 s60, -2
	s_mov_b64 s[20:21], s[12:13]
	v_mov_b32_e32 v3, v2
	v_mov_b32_e32 v4, v2
	v_mov_b32_e32 v5, v2
	v_mov_b32_e32 v10, v2
	v_mov_b32_e32 v11, v2
	v_mov_b32_e32 v12, v2
	v_mov_b32_e32 v13, v2
	v_mov_b32_e32 v18, v2
	v_mov_b32_e32 v19, v2
	v_mov_b32_e32 v20, v2
	v_mov_b32_e32 v21, v2
	v_mov_b32_e32 v26, v2
	v_mov_b32_e32 v27, v2
	v_mov_b32_e32 v28, v2
	v_mov_b32_e32 v29, v2
	v_mov_b32_e32 v42, v2
	v_mov_b32_e32 v43, v2
	v_mov_b32_e32 v44, v2
	v_mov_b32_e32 v45, v2
	v_mov_b32_e32 v54, v2
	v_mov_b32_e32 v55, v2
	v_mov_b32_e32 v56, v2
	v_mov_b32_e32 v57, v2
	v_mov_b32_e32 v70, v2
	v_mov_b32_e32 v71, v2
	v_mov_b32_e32 v72, v2
	v_mov_b32_e32 v73, v2
	v_mov_b32_e32 v86, v2
	v_mov_b32_e32 v87, v2
	v_mov_b32_e32 v88, v2
	v_mov_b32_e32 v89, v2
	v_mov_b32_e32 v6, v2
	v_mov_b32_e32 v7, v2
	v_mov_b32_e32 v8, v2
	v_mov_b32_e32 v9, v2
	v_mov_b32_e32 v14, v2
	v_mov_b32_e32 v15, v2
	v_mov_b32_e32 v16, v2
	v_mov_b32_e32 v17, v2
	v_mov_b32_e32 v22, v2
	v_mov_b32_e32 v23, v2
	v_mov_b32_e32 v24, v2
	v_mov_b32_e32 v25, v2
	v_mov_b32_e32 v30, v2
	v_mov_b32_e32 v31, v2
	v_mov_b32_e32 v32, v2
	v_mov_b32_e32 v33, v2
	v_mov_b32_e32 v50, v2
	v_mov_b32_e32 v51, v2
	v_mov_b32_e32 v52, v2
	v_mov_b32_e32 v53, v2
	v_mov_b32_e32 v58, v2
	v_mov_b32_e32 v59, v2
	v_mov_b32_e32 v60, v2
	v_mov_b32_e32 v61, v2
	v_mov_b32_e32 v78, v2
	v_mov_b32_e32 v79, v2
	v_mov_b32_e32 v80, v2
	v_mov_b32_e32 v81, v2
	v_mov_b32_e32 v90, v2
	v_mov_b32_e32 v91, v2
	v_mov_b32_e32 v92, v2
	v_mov_b32_e32 v93, v2
	v_mov_b32_e32 v34, v2
	v_mov_b32_e32 v35, v2
	v_mov_b32_e32 v36, v2
	v_mov_b32_e32 v37, v2
	v_mov_b32_e32 v38, v2
	v_mov_b32_e32 v39, v2
	v_mov_b32_e32 v40, v2
	v_mov_b32_e32 v41, v2
	v_mov_b32_e32 v66, v2
	v_mov_b32_e32 v67, v2
	v_mov_b32_e32 v68, v2
	v_mov_b32_e32 v69, v2
	v_mov_b32_e32 v74, v2
	v_mov_b32_e32 v75, v2
	v_mov_b32_e32 v76, v2
	v_mov_b32_e32 v77, v2
	v_mov_b32_e32 v98, v2
	v_mov_b32_e32 v99, v2
	v_mov_b32_e32 v100, v2
	v_mov_b32_e32 v101, v2
	v_mov_b32_e32 v102, v2
	v_mov_b32_e32 v103, v2
	v_mov_b32_e32 v104, v2
	v_mov_b32_e32 v105, v2
	v_mov_b32_e32 v114, v2
	v_mov_b32_e32 v115, v2
	v_mov_b32_e32 v116, v2
	v_mov_b32_e32 v117, v2
	v_mov_b32_e32 v118, v2
	v_mov_b32_e32 v119, v2
	v_mov_b32_e32 v120, v2
	v_mov_b32_e32 v121, v2
	v_mov_b32_e32 v46, v2
	v_mov_b32_e32 v47, v2
	v_mov_b32_e32 v48, v2
	v_mov_b32_e32 v49, v2
	v_mov_b32_e32 v62, v2
	v_mov_b32_e32 v63, v2
	v_mov_b32_e32 v64, v2
	v_mov_b32_e32 v65, v2
	v_mov_b32_e32 v82, v2
	v_mov_b32_e32 v83, v2
	v_mov_b32_e32 v84, v2
	v_mov_b32_e32 v85, v2
	v_mov_b32_e32 v94, v2
	v_mov_b32_e32 v95, v2
	v_mov_b32_e32 v96, v2
	v_mov_b32_e32 v97, v2
	v_mov_b32_e32 v106, v2
	v_mov_b32_e32 v107, v2
	v_mov_b32_e32 v108, v2
	v_mov_b32_e32 v109, v2
	v_mov_b32_e32 v110, v2
	v_mov_b32_e32 v111, v2
	v_mov_b32_e32 v112, v2
	v_mov_b32_e32 v113, v2
	v_mov_b32_e32 v122, v2
	v_mov_b32_e32 v123, v2
	v_mov_b32_e32 v124, v2
	v_mov_b32_e32 v125, v2
	v_mov_b32_e32 v126, v2
	v_mov_b32_e32 v127, v2
	v_mov_b32_e32 v128, v2
	v_mov_b32_e32 v129, v2
	.p2align 6

.LBB0_1478:
	s_ashr_i32 s21, s20, 31
	s_lshl_b64 s[22:23], s[20:21], 19
	s_add_u32 s22, s2, s22
	s_addc_u32 s23, s3, s23
	s_and_b64 s[30:31], s[4:5], exec
	s_cselect_b32 s9, s23, s7
	s_cselect_b32 s21, s22, s6
	s_ashr_i32 s19, s18, 31
	s_lshl_b64 s[30:31], s[18:19], 19
	s_add_u32 s30, s96, s30
	s_addc_u32 s31, s97, s31
	s_and_b64 s[38:39], s[4:5], exec
	s_cselect_b32 s19, s31, s37
	s_cselect_b32 s35, s30, s36
	s_add_u32 s6, s6, 0x40080
	s_addc_u32 s7, s7, 0
	s_add_u32 s64, s36, 0x100
	v_mov_b32_e32 v2, 0
	s_addc_u32 s65, s37, 0
	s_mov_b32 s66, -2
	v_mov_b32_e32 v3, v2
	v_mov_b32_e32 v4, v2
	v_mov_b32_e32 v5, v2
	v_mov_b32_e32 v6, v2
	v_mov_b32_e32 v7, v2
	v_mov_b32_e32 v8, v2
	v_mov_b32_e32 v9, v2
	v_mov_b32_e32 v18, v2
	v_mov_b32_e32 v19, v2
	v_mov_b32_e32 v20, v2
	v_mov_b32_e32 v21, v2
	v_mov_b32_e32 v22, v2
	v_mov_b32_e32 v23, v2
	v_mov_b32_e32 v24, v2
	v_mov_b32_e32 v25, v2
	v_mov_b32_e32 v34, v2
	v_mov_b32_e32 v35, v2
	v_mov_b32_e32 v36, v2
	v_mov_b32_e32 v37, v2
	v_mov_b32_e32 v38, v2
	v_mov_b32_e32 v39, v2
	v_mov_b32_e32 v40, v2
	v_mov_b32_e32 v41, v2
	v_mov_b32_e32 v50, v2
	v_mov_b32_e32 v51, v2
	v_mov_b32_e32 v52, v2
	v_mov_b32_e32 v53, v2
	v_mov_b32_e32 v54, v2
	v_mov_b32_e32 v55, v2
	v_mov_b32_e32 v56, v2
	v_mov_b32_e32 v57, v2
	v_mov_b32_e32 v10, v2
	v_mov_b32_e32 v11, v2
	v_mov_b32_e32 v12, v2
	v_mov_b32_e32 v13, v2
	v_mov_b32_e32 v14, v2
	v_mov_b32_e32 v15, v2
	v_mov_b32_e32 v16, v2
	v_mov_b32_e32 v17, v2
	v_mov_b32_e32 v26, v2
	v_mov_b32_e32 v27, v2
	v_mov_b32_e32 v28, v2
	v_mov_b32_e32 v29, v2
	v_mov_b32_e32 v30, v2
	v_mov_b32_e32 v31, v2
	v_mov_b32_e32 v32, v2
	v_mov_b32_e32 v33, v2
	v_mov_b32_e32 v42, v2
	v_mov_b32_e32 v43, v2
	v_mov_b32_e32 v44, v2
	v_mov_b32_e32 v45, v2
	v_mov_b32_e32 v46, v2
	v_mov_b32_e32 v47, v2
	v_mov_b32_e32 v48, v2
	v_mov_b32_e32 v49, v2
	v_mov_b32_e32 v58, v2
	v_mov_b32_e32 v59, v2
	v_mov_b32_e32 v60, v2
	v_mov_b32_e32 v61, v2
	v_mov_b32_e32 v62, v2
	v_mov_b32_e32 v63, v2
	v_mov_b32_e32 v64, v2
	v_mov_b32_e32 v65, v2
	v_mov_b32_e32 v82, v2
	v_mov_b32_e32 v83, v2
	v_mov_b32_e32 v84, v2
	v_mov_b32_e32 v85, v2
	v_mov_b32_e32 v86, v2
	v_mov_b32_e32 v87, v2
	v_mov_b32_e32 v88, v2
	v_mov_b32_e32 v89, v2
	v_mov_b32_e32 v98, v2
	v_mov_b32_e32 v99, v2
	v_mov_b32_e32 v100, v2
	v_mov_b32_e32 v101, v2
	v_mov_b32_e32 v102, v2
	v_mov_b32_e32 v103, v2
	v_mov_b32_e32 v104, v2
	v_mov_b32_e32 v105, v2
	v_mov_b32_e32 v114, v2
	v_mov_b32_e32 v115, v2
	v_mov_b32_e32 v116, v2
	v_mov_b32_e32 v117, v2
	v_mov_b32_e32 v118, v2
	v_mov_b32_e32 v119, v2
	v_mov_b32_e32 v120, v2
	v_mov_b32_e32 v121, v2
	v_mov_b32_e32 v130, v2
	v_mov_b32_e32 v131, v2
	v_mov_b32_e32 v132, v2
	v_mov_b32_e32 v133, v2
	v_mov_b32_e32 v134, v2
	v_mov_b32_e32 v135, v2
	v_mov_b32_e32 v136, v2
	v_mov_b32_e32 v137, v2
	v_mov_b32_e32 v90, v2
	v_mov_b32_e32 v91, v2
	v_mov_b32_e32 v92, v2
	v_mov_b32_e32 v93, v2
	v_mov_b32_e32 v94, v2
	v_mov_b32_e32 v95, v2
	v_mov_b32_e32 v96, v2
	v_mov_b32_e32 v97, v2
	v_mov_b32_e32 v106, v2
	v_mov_b32_e32 v107, v2
	v_mov_b32_e32 v108, v2
	v_mov_b32_e32 v109, v2
	v_mov_b32_e32 v110, v2
	v_mov_b32_e32 v111, v2
	v_mov_b32_e32 v112, v2
	v_mov_b32_e32 v113, v2
	v_mov_b32_e32 v122, v2
	v_mov_b32_e32 v123, v2
	v_mov_b32_e32 v124, v2
	v_mov_b32_e32 v125, v2
	v_mov_b32_e32 v126, v2
	v_mov_b32_e32 v127, v2
	v_mov_b32_e32 v128, v2
	v_mov_b32_e32 v129, v2
	v_mov_b32_e32 v138, v2
	v_mov_b32_e32 v139, v2
	v_mov_b32_e32 v140, v2
	v_mov_b32_e32 v141, v2
	v_mov_b32_e32 v142, v2
	v_mov_b32_e32 v143, v2
	v_mov_b32_e32 v144, v2
	v_mov_b32_e32 v145, v2
	.p2align 6

.LBB0_1598:
	s_ashr_i32 s21, s20, 31
	s_lshl_b64 s[22:23], s[20:21], 19
	s_add_u32 s22, s2, s22
	s_addc_u32 s23, s3, s23
	s_and_b64 s[30:31], s[4:5], exec
	s_cselect_b32 s21, s23, s37
	s_cselect_b32 s60, s22, s36
	s_ashr_i32 s19, s18, 31
	s_lshl_b64 s[30:31], s[18:19], 19
	s_add_u32 s30, s90, s30
	s_addc_u32 s31, s91, s31
	s_and_b64 s[40:41], s[4:5], exec
	s_cselect_b32 s19, s31, s39
	s_cselect_b32 s61, s30, s38
	s_add_u32 s36, s36, 0x40080
	s_addc_u32 s37, s37, 0
	s_add_u32 s62, s38, 0x100
	v_mov_b32_e32 v2, 0
	s_addc_u32 s63, s39, 0
	s_mov_b32 s64, -2
	v_mov_b32_e32 v3, v2
	v_mov_b32_e32 v4, v2
	v_mov_b32_e32 v5, v2
	v_mov_b32_e32 v6, v2
	v_mov_b32_e32 v7, v2
	v_mov_b32_e32 v8, v2
	v_mov_b32_e32 v9, v2
	v_mov_b32_e32 v14, v2
	v_mov_b32_e32 v15, v2
	v_mov_b32_e32 v16, v2
	v_mov_b32_e32 v17, v2
	v_mov_b32_e32 v22, v2
	v_mov_b32_e32 v23, v2
	v_mov_b32_e32 v24, v2
	v_mov_b32_e32 v25, v2
	v_mov_b32_e32 v30, v2
	v_mov_b32_e32 v31, v2
	v_mov_b32_e32 v32, v2
	v_mov_b32_e32 v33, v2
	v_mov_b32_e32 v38, v2
	v_mov_b32_e32 v39, v2
	v_mov_b32_e32 v40, v2
	v_mov_b32_e32 v41, v2
	v_mov_b32_e32 v46, v2
	v_mov_b32_e32 v47, v2
	v_mov_b32_e32 v48, v2
	v_mov_b32_e32 v49, v2
	v_mov_b32_e32 v54, v2
	v_mov_b32_e32 v55, v2
	v_mov_b32_e32 v56, v2
	v_mov_b32_e32 v57, v2
	v_mov_b32_e32 v10, v2
	v_mov_b32_e32 v11, v2
	v_mov_b32_e32 v12, v2
	v_mov_b32_e32 v13, v2
	v_mov_b32_e32 v18, v2
	v_mov_b32_e32 v19, v2
	v_mov_b32_e32 v20, v2
	v_mov_b32_e32 v21, v2
	v_mov_b32_e32 v26, v2
	v_mov_b32_e32 v27, v2
	v_mov_b32_e32 v28, v2
	v_mov_b32_e32 v29, v2
	v_mov_b32_e32 v34, v2
	v_mov_b32_e32 v35, v2
	v_mov_b32_e32 v36, v2
	v_mov_b32_e32 v37, v2
	v_mov_b32_e32 v42, v2
	v_mov_b32_e32 v43, v2
	v_mov_b32_e32 v44, v2
	v_mov_b32_e32 v45, v2
	v_mov_b32_e32 v50, v2
	v_mov_b32_e32 v51, v2
	v_mov_b32_e32 v52, v2
	v_mov_b32_e32 v53, v2
	v_mov_b32_e32 v58, v2
	v_mov_b32_e32 v59, v2
	v_mov_b32_e32 v60, v2
	v_mov_b32_e32 v61, v2
	v_mov_b32_e32 v62, v2
	v_mov_b32_e32 v63, v2
	v_mov_b32_e32 v64, v2
	v_mov_b32_e32 v65, v2
	v_mov_b32_e32 v66, v2
	v_mov_b32_e32 v67, v2
	v_mov_b32_e32 v68, v2
	v_mov_b32_e32 v69, v2
	v_mov_b32_e32 v70, v2
	v_mov_b32_e32 v71, v2
	v_mov_b32_e32 v72, v2
	v_mov_b32_e32 v73, v2
	v_mov_b32_e32 v78, v2
	v_mov_b32_e32 v79, v2
	v_mov_b32_e32 v80, v2
	v_mov_b32_e32 v81, v2
	v_mov_b32_e32 v86, v2
	v_mov_b32_e32 v87, v2
	v_mov_b32_e32 v88, v2
	v_mov_b32_e32 v89, v2
	v_mov_b32_e32 v94, v2
	v_mov_b32_e32 v95, v2
	v_mov_b32_e32 v96, v2
	v_mov_b32_e32 v97, v2
	v_mov_b32_e32 v102, v2
	v_mov_b32_e32 v103, v2
	v_mov_b32_e32 v104, v2
	v_mov_b32_e32 v105, v2
	v_mov_b32_e32 v110, v2
	v_mov_b32_e32 v111, v2
	v_mov_b32_e32 v112, v2
	v_mov_b32_e32 v113, v2
	v_mov_b32_e32 v118, v2
	v_mov_b32_e32 v119, v2
	v_mov_b32_e32 v120, v2
	v_mov_b32_e32 v121, v2
	v_mov_b32_e32 v74, v2
	v_mov_b32_e32 v75, v2
	v_mov_b32_e32 v76, v2
	v_mov_b32_e32 v77, v2
	v_mov_b32_e32 v82, v2
	v_mov_b32_e32 v83, v2
	v_mov_b32_e32 v84, v2
	v_mov_b32_e32 v85, v2
	v_mov_b32_e32 v90, v2
	v_mov_b32_e32 v91, v2
	v_mov_b32_e32 v92, v2
	v_mov_b32_e32 v93, v2
	v_mov_b32_e32 v98, v2
	v_mov_b32_e32 v99, v2
	v_mov_b32_e32 v100, v2
	v_mov_b32_e32 v101, v2
	v_mov_b32_e32 v106, v2
	v_mov_b32_e32 v107, v2
	v_mov_b32_e32 v108, v2
	v_mov_b32_e32 v109, v2
	v_mov_b32_e32 v114, v2
	v_mov_b32_e32 v115, v2
	v_mov_b32_e32 v116, v2
	v_mov_b32_e32 v117, v2
	v_mov_b32_e32 v122, v2
	v_mov_b32_e32 v123, v2
	v_mov_b32_e32 v124, v2
	v_mov_b32_e32 v125, v2
	v_mov_b32_e32 v126, v2
	v_mov_b32_e32 v127, v2
	v_mov_b32_e32 v128, v2
	v_mov_b32_e32 v129, v2
	.p2align 6

.LBB0_1700:
	s_cmp_lg_u32 0, -1
	s_waitcnt vmcnt(0) lgkmcnt(0)
	s_barrier
	s_cselect_b32 s9, 0, 0
	s_nop 8
	v_exp_f32_e32 v50, v2
	v_exp_f32_e32 v51, v3
	v_lshl_add_u64 v[2:3], v[214:215], 0, s[16:17]
	s_mov_b32 s8, m0
	s_mov_b32 m0, s50
	s_nop 0
	global_load_lds_dwordx4 v[2:3], off
	s_mov_b32 m0, s8
	s_add_i32 s9, s9, s30
	v_lshl_add_u64 v[216:217], v[34:35], 0, s[12:13]
	s_add_i32 s9, s9, 0x8000
	s_mov_b32 s30, m0
	s_mov_b32 m0, s9
	s_nop 0
	global_load_lds_dwordx4 v[216:217], off
	s_mov_b32 m0, s30
	ds_read_b128 v[174:177], v232 offset:8192
	ds_read_b128 v[166:169], v232 offset:8704
	ds_read_b128 v[170:173], v232 offset:10240
	ds_read_b128 v[158:161], v232 offset:10752
	ds_read_b128 v[162:165], v232 offset:12288
	ds_read_b128 v[150:153], v232 offset:12800
	ds_read_b128 v[154:157], v232 offset:14336
	ds_read_b128 v[146:149], v232 offset:14848
	v_exp_f32_e32 v66, v18
	v_exp_f32_e32 v67, v19
	v_exp_f32_e32 v68, v20
	v_exp_f32_e32 v69, v21
	v_exp_f32_e32 v70, v22
	v_exp_f32_e32 v71, v23
	v_exp_f32_e32 v72, v24
	v_exp_f32_e32 v73, v25
	v_exp_f32_e32 v74, v26
	v_exp_f32_e32 v75, v27
	v_exp_f32_e32 v76, v28
	v_exp_f32_e32 v77, v29
	v_exp_f32_e32 v78, v30
	v_exp_f32_e32 v79, v31
	v_exp_f32_e32 v80, v32
	v_exp_f32_e32 v81, v33
	v_exp_f32_e32 v52, v4
	v_exp_f32_e32 v53, v5
	v_exp_f32_e32 v54, v6
	v_exp_f32_e32 v55, v7
	v_exp_f32_e32 v56, v8
	v_exp_f32_e32 v57, v9
	v_exp_f32_e32 v58, v10
	v_exp_f32_e32 v59, v11
	v_exp_f32_e32 v60, v12
	v_exp_f32_e32 v61, v13
	v_exp_f32_e32 v62, v14
	v_exp_f32_e32 v63, v15
	v_exp_f32_e32 v64, v16
	v_exp_f32_e32 v65, v17
	s_waitcnt vmcnt(2) lgkmcnt(0)
	s_barrier
	s_mov_b32 s8, 0
	s_cmp_lt_i32 s49, 7
	s_mov_b32 s42, 0
	s_cbranch_scc1 .LBB0_1741
	v_lshl_add_u64 v[218:219], v[34:35], 0, s[16:17]
	v_mov_b32_e32 v34, 0
	s_add_i32 s9, s49, -5
	v_lshl_add_u64 v[220:221], v[214:215], 0, s[18:19]
	s_mov_b32 s30, 1
	s_movk_i32 s53, 0x4000
	s_movk_i32 s52, 0x2000
	v_mov_b32_e32 v35, v241
	v_mov_b32_e32 v2, 0
	v_mov_b32_e32 v3, v34
	v_mov_b32_e32 v4, v34
	v_mov_b32_e32 v5, v34
	v_mov_b32_e32 v6, v34
	v_mov_b32_e32 v7, v34
	v_mov_b32_e32 v8, v34
	v_mov_b32_e32 v9, v34
	v_mov_b32_e32 v10, v34
	v_mov_b32_e32 v11, v34
	v_mov_b32_e32 v12, v34
	v_mov_b32_e32 v13, v34
	v_mov_b32_e32 v14, v34
	v_mov_b32_e32 v15, v34
	v_mov_b32_e32 v16, v34
	v_mov_b32_e32 v17, v34
	v_mov_b32_e32 v18, 0
	v_mov_b32_e32 v19, v34
	v_mov_b32_e32 v20, v34
	v_mov_b32_e32 v21, v34
	v_mov_b32_e32 v22, v34
	v_mov_b32_e32 v23, v34
	v_mov_b32_e32 v24, v34
	v_mov_b32_e32 v25, v34
	v_mov_b32_e32 v26, v34
	v_mov_b32_e32 v27, v34
	v_mov_b32_e32 v28, v34
	v_mov_b32_e32 v29, v34
	v_mov_b32_e32 v30, v34
	v_mov_b32_e32 v31, v34
	v_mov_b32_e32 v32, v34
	v_mov_b32_e32 v33, v34
	.p2align 6

.LBB0_1704:
	v_lshl_add_u32 v35, s30, 6, v237
	v_subrev_u32_e32 v35, s40, v35
	s_lshl_b64 s[40:41], s[30:31], 17
	v_lshl_add_u64 v[36:37], v[214:215], 0, s[40:41]
	s_add_i32 s56, s49, -2
	s_sub_i32 s57, 0, s49
	s_add_i32 s60, s30, 2
	v_lshl_add_u32 v218, s30, 8, v233
	v_lshl_add_u64 v[48:49], v[216:217], 0, s[40:41]
	v_lshl_add_u64 v[214:215], v[36:37], 0, s[22:23]
	.p2align 6

.LBB0_1882:
	s_ashr_i32 s15, s14, 31
	s_lshl_b64 s[16:17], s[14:15], 19
	s_add_u32 s16, s28, s16
	s_addc_u32 s17, s29, s17
	s_and_b64 s[18:19], s[4:5], exec
	s_cselect_b32 s15, s17, s23
	s_cselect_b32 s48, s16, s22
	s_ashr_i32 s13, s12, 31
	s_lshl_b64 s[18:19], s[12:13], 19
	s_add_u32 s18, s86, s18
	s_addc_u32 s19, s87, s19
	s_and_b64 s[34:35], s[4:5], exec
	s_cselect_b32 s13, s19, s31
	s_cselect_b32 s49, s18, s30
	s_add_u32 s22, s22, 0x40080
	s_addc_u32 s23, s23, 0
	s_add_u32 s50, s30, 0x100
	v_mov_b32_e32 v2, 0
	s_addc_u32 s51, s31, 0
	s_mov_b32 s52, -2
	v_mov_b32_e32 v3, v2
	v_mov_b32_e32 v4, v2
	v_mov_b32_e32 v5, v2
	v_mov_b32_e32 v6, v2
	v_mov_b32_e32 v7, v2
	v_mov_b32_e32 v8, v2
	v_mov_b32_e32 v9, v2
	v_mov_b32_e32 v14, v2
	v_mov_b32_e32 v15, v2
	v_mov_b32_e32 v16, v2
	v_mov_b32_e32 v17, v2
	v_mov_b32_e32 v22, v2
	v_mov_b32_e32 v23, v2
	v_mov_b32_e32 v24, v2
	v_mov_b32_e32 v25, v2
	v_mov_b32_e32 v30, v2
	v_mov_b32_e32 v31, v2
	v_mov_b32_e32 v32, v2
	v_mov_b32_e32 v33, v2
	v_mov_b32_e32 v38, v2
	v_mov_b32_e32 v39, v2
	v_mov_b32_e32 v40, v2
	v_mov_b32_e32 v41, v2
	v_mov_b32_e32 v46, v2
	v_mov_b32_e32 v47, v2
	v_mov_b32_e32 v48, v2
	v_mov_b32_e32 v49, v2
	v_mov_b32_e32 v54, v2
	v_mov_b32_e32 v55, v2
	v_mov_b32_e32 v56, v2
	v_mov_b32_e32 v57, v2
	v_mov_b32_e32 v10, v2
	v_mov_b32_e32 v11, v2
	v_mov_b32_e32 v12, v2
	v_mov_b32_e32 v13, v2
	v_mov_b32_e32 v18, v2
	v_mov_b32_e32 v19, v2
	v_mov_b32_e32 v20, v2
	v_mov_b32_e32 v21, v2
	v_mov_b32_e32 v26, v2
	v_mov_b32_e32 v27, v2
	v_mov_b32_e32 v28, v2
	v_mov_b32_e32 v29, v2
	v_mov_b32_e32 v34, v2
	v_mov_b32_e32 v35, v2
	v_mov_b32_e32 v36, v2
	v_mov_b32_e32 v37, v2
	v_mov_b32_e32 v42, v2
	v_mov_b32_e32 v43, v2
	v_mov_b32_e32 v44, v2
	v_mov_b32_e32 v45, v2
	v_mov_b32_e32 v50, v2
	v_mov_b32_e32 v51, v2
	v_mov_b32_e32 v52, v2
	v_mov_b32_e32 v53, v2
	v_mov_b32_e32 v58, v2
	v_mov_b32_e32 v59, v2
	v_mov_b32_e32 v60, v2
	v_mov_b32_e32 v61, v2
	v_mov_b32_e32 v62, v2
	v_mov_b32_e32 v63, v2
	v_mov_b32_e32 v64, v2
	v_mov_b32_e32 v65, v2
	v_mov_b32_e32 v66, v2
	v_mov_b32_e32 v67, v2
	v_mov_b32_e32 v68, v2
	v_mov_b32_e32 v69, v2
	v_mov_b32_e32 v70, v2
	v_mov_b32_e32 v71, v2
	v_mov_b32_e32 v72, v2
	v_mov_b32_e32 v73, v2
	v_mov_b32_e32 v78, v2
	v_mov_b32_e32 v79, v2
	v_mov_b32_e32 v80, v2
	v_mov_b32_e32 v81, v2
	v_mov_b32_e32 v86, v2
	v_mov_b32_e32 v87, v2
	v_mov_b32_e32 v88, v2
	v_mov_b32_e32 v89, v2
	v_mov_b32_e32 v94, v2
	v_mov_b32_e32 v95, v2
	v_mov_b32_e32 v96, v2
	v_mov_b32_e32 v97, v2
	v_mov_b32_e32 v102, v2
	v_mov_b32_e32 v103, v2
	v_mov_b32_e32 v104, v2
	v_mov_b32_e32 v105, v2
	v_mov_b32_e32 v110, v2
	v_mov_b32_e32 v111, v2
	v_mov_b32_e32 v112, v2
	v_mov_b32_e32 v113, v2
	v_mov_b32_e32 v118, v2
	v_mov_b32_e32 v119, v2
	v_mov_b32_e32 v120, v2
	v_mov_b32_e32 v121, v2
	v_mov_b32_e32 v74, v2
	v_mov_b32_e32 v75, v2
	v_mov_b32_e32 v76, v2
	v_mov_b32_e32 v77, v2
	v_mov_b32_e32 v82, v2
	v_mov_b32_e32 v83, v2
	v_mov_b32_e32 v84, v2
	v_mov_b32_e32 v85, v2
	v_mov_b32_e32 v90, v2
	v_mov_b32_e32 v91, v2
	v_mov_b32_e32 v92, v2
	v_mov_b32_e32 v93, v2
	v_mov_b32_e32 v98, v2
	v_mov_b32_e32 v99, v2
	v_mov_b32_e32 v100, v2
	v_mov_b32_e32 v101, v2
	v_mov_b32_e32 v106, v2
	v_mov_b32_e32 v107, v2
	v_mov_b32_e32 v108, v2
	v_mov_b32_e32 v109, v2
	v_mov_b32_e32 v114, v2
	v_mov_b32_e32 v115, v2
	v_mov_b32_e32 v116, v2
	v_mov_b32_e32 v117, v2
	v_mov_b32_e32 v122, v2
	v_mov_b32_e32 v123, v2
	v_mov_b32_e32 v124, v2
	v_mov_b32_e32 v125, v2
	v_mov_b32_e32 v126, v2
	v_mov_b32_e32 v127, v2
	v_mov_b32_e32 v128, v2
	v_mov_b32_e32 v129, v2
	.p2align 6

.LBB0_2068:
	s_and_b64 s[14:15], s[14:15], exec
	s_cselect_b32 s55, s49, s54
	s_cmpk_gt_i32 s52, 0x80
	s_cselect_b64 s[14:15], -1, 0
	s_add_u32 s56, s16, 0x100
	v_lshl_add_u32 v165, s54, 2, v149
	s_addc_u32 s57, s17, 0
	s_mov_b64 s[18:19], -1
	s_and_b64 vcc, exec, s[14:15]
	s_cbranch_vccnz .LBB0_2072
	s_add_u32 s58, s16, 0x100
	v_mov_b32_e32 v2, 0
	s_addc_u32 s59, s17, 0
	s_mov_b32 s62, -2
	s_mov_b64 s[16:17], s[8:9]
	v_mov_b32_e32 v3, v2
	v_mov_b32_e32 v4, v2
	v_mov_b32_e32 v5, v2
	v_mov_b32_e32 v6, v2
	v_mov_b32_e32 v7, v2
	v_mov_b32_e32 v8, v2
	v_mov_b32_e32 v9, v2
	v_mov_b32_e32 v34, v2
	v_mov_b32_e32 v35, v2
	v_mov_b32_e32 v36, v2
	v_mov_b32_e32 v37, v2
	v_mov_b32_e32 v38, v2
	v_mov_b32_e32 v39, v2
	v_mov_b32_e32 v40, v2
	v_mov_b32_e32 v41, v2
	v_mov_b32_e32 v66, v2
	v_mov_b32_e32 v67, v2
	v_mov_b32_e32 v68, v2
	v_mov_b32_e32 v69, v2
	v_mov_b32_e32 v70, v2
	v_mov_b32_e32 v71, v2
	v_mov_b32_e32 v72, v2
	v_mov_b32_e32 v73, v2
	v_mov_b32_e32 v98, v2
	v_mov_b32_e32 v99, v2
	v_mov_b32_e32 v100, v2
	v_mov_b32_e32 v101, v2
	v_mov_b32_e32 v102, v2
	v_mov_b32_e32 v103, v2
	v_mov_b32_e32 v104, v2
	v_mov_b32_e32 v105, v2
	v_mov_b32_e32 v10, v2
	v_mov_b32_e32 v11, v2
	v_mov_b32_e32 v12, v2
	v_mov_b32_e32 v13, v2
	v_mov_b32_e32 v18, v2
	v_mov_b32_e32 v19, v2
	v_mov_b32_e32 v20, v2
	v_mov_b32_e32 v21, v2
	v_mov_b32_e32 v42, v2
	v_mov_b32_e32 v43, v2
	v_mov_b32_e32 v44, v2
	v_mov_b32_e32 v45, v2
	v_mov_b32_e32 v54, v2
	v_mov_b32_e32 v55, v2
	v_mov_b32_e32 v56, v2
	v_mov_b32_e32 v57, v2
	v_mov_b32_e32 v82, v2
	v_mov_b32_e32 v83, v2
	v_mov_b32_e32 v84, v2
	v_mov_b32_e32 v85, v2
	v_mov_b32_e32 v94, v2
	v_mov_b32_e32 v95, v2
	v_mov_b32_e32 v96, v2
	v_mov_b32_e32 v97, v2
	v_mov_b32_e32 v122, v2
	v_mov_b32_e32 v123, v2
	v_mov_b32_e32 v124, v2
	v_mov_b32_e32 v125, v2
	v_mov_b32_e32 v126, v2
	v_mov_b32_e32 v127, v2
	v_mov_b32_e32 v128, v2
	v_mov_b32_e32 v129, v2
	.p2align 6

.LBB0_2072:
	v_mov_b32_e32 v121, 0
	s_and_b64 vcc, exec, s[18:19]
	v_mov_b32_e32 v120, v121
	v_mov_b32_e32 v119, v121
	v_mov_b32_e32 v118, v121
	v_mov_b32_e32 v117, v121
	v_mov_b32_e32 v116, v121
	v_mov_b32_e32 v115, v121
	v_mov_b32_e32 v114, v121
	v_mov_b32_e32 v93, v121
	v_mov_b32_e32 v92, v121
	v_mov_b32_e32 v91, v121
	v_mov_b32_e32 v90, v121
	v_mov_b32_e32 v89, v121
	v_mov_b32_e32 v88, v121
	v_mov_b32_e32 v87, v121
	v_mov_b32_e32 v86, v121
	v_mov_b32_e32 v65, v121
	v_mov_b32_e32 v64, v121
	v_mov_b32_e32 v63, v121
	v_mov_b32_e32 v62, v121
	v_mov_b32_e32 v61, v121
	v_mov_b32_e32 v60, v121
	v_mov_b32_e32 v59, v121
	v_mov_b32_e32 v58, v121
	v_mov_b32_e32 v33, v121
	v_mov_b32_e32 v32, v121
	v_mov_b32_e32 v31, v121
	v_mov_b32_e32 v30, v121
	v_mov_b32_e32 v29, v121
	v_mov_b32_e32 v28, v121
	v_mov_b32_e32 v27, v121
	v_mov_b32_e32 v26, v121
	v_mov_b32_e32 v113, v121
	v_mov_b32_e32 v112, v121
	v_mov_b32_e32 v111, v121
	v_mov_b32_e32 v110, v121
	v_mov_b32_e32 v109, v121
	v_mov_b32_e32 v108, v121
	v_mov_b32_e32 v107, v121
	v_mov_b32_e32 v106, v121
	v_mov_b32_e32 v81, v121
	v_mov_b32_e32 v80, v121
	v_mov_b32_e32 v79, v121
	v_mov_b32_e32 v78, v121
	v_mov_b32_e32 v77, v121
	v_mov_b32_e32 v76, v121
	v_mov_b32_e32 v75, v121
	v_mov_b32_e32 v74, v121
	v_mov_b32_e32 v53, v121
	v_mov_b32_e32 v52, v121
	v_mov_b32_e32 v51, v121
	v_mov_b32_e32 v50, v121
	v_mov_b32_e32 v49, v121
	v_mov_b32_e32 v48, v121
	v_mov_b32_e32 v47, v121
	v_mov_b32_e32 v46, v121
	v_mov_b32_e32 v25, v121
	v_mov_b32_e32 v24, v121
	v_mov_b32_e32 v23, v121
	v_mov_b32_e32 v22, v121
	v_mov_b32_e32 v17, v121
	v_mov_b32_e32 v16, v121
	v_mov_b32_e32 v15, v121
	v_mov_b32_e32 v14, v121
	s_cbranch_vccz .LBB0_2075
	v_mov_b32_e32 v14, 0
	s_mov_b32 s58, -2
	s_mov_b64 s[16:17], s[8:9]
	v_mov_b32_e32 v15, v14
	v_mov_b32_e32 v16, v14
	v_mov_b32_e32 v17, v14
	v_mov_b32_e32 v22, v14
	v_mov_b32_e32 v23, v14
	v_mov_b32_e32 v24, v14
	v_mov_b32_e32 v25, v14
	v_mov_b32_e32 v46, v14
	v_mov_b32_e32 v47, v14
	v_mov_b32_e32 v48, v14
	v_mov_b32_e32 v49, v14
	v_mov_b32_e32 v50, v14
	v_mov_b32_e32 v51, v14
	v_mov_b32_e32 v52, v14
	v_mov_b32_e32 v53, v14
	v_mov_b32_e32 v74, v14
	v_mov_b32_e32 v75, v14
	v_mov_b32_e32 v76, v14
	v_mov_b32_e32 v77, v14
	v_mov_b32_e32 v78, v14
	v_mov_b32_e32 v79, v14
	v_mov_b32_e32 v80, v14
	v_mov_b32_e32 v81, v14
	v_mov_b32_e32 v106, v14
	v_mov_b32_e32 v107, v14
	v_mov_b32_e32 v108, v14
	v_mov_b32_e32 v109, v14
	v_mov_b32_e32 v110, v14
	v_mov_b32_e32 v111, v14
	v_mov_b32_e32 v112, v14
	v_mov_b32_e32 v113, v14
	v_mov_b32_e32 v26, v14
	v_mov_b32_e32 v27, v14
	v_mov_b32_e32 v28, v14
	v_mov_b32_e32 v29, v14
	v_mov_b32_e32 v30, v14
	v_mov_b32_e32 v31, v14
	v_mov_b32_e32 v32, v14
	v_mov_b32_e32 v33, v14
	v_mov_b32_e32 v58, v14
	v_mov_b32_e32 v59, v14
	v_mov_b32_e32 v60, v14
	v_mov_b32_e32 v61, v14
	v_mov_b32_e32 v62, v14
	v_mov_b32_e32 v63, v14
	v_mov_b32_e32 v64, v14
	v_mov_b32_e32 v65, v14
	v_mov_b32_e32 v86, v14
	v_mov_b32_e32 v87, v14
	v_mov_b32_e32 v88, v14
	v_mov_b32_e32 v89, v14
	v_mov_b32_e32 v90, v14
	v_mov_b32_e32 v91, v14
	v_mov_b32_e32 v92, v14
	v_mov_b32_e32 v93, v14
	v_mov_b32_e32 v114, v14
	v_mov_b32_e32 v115, v14
	v_mov_b32_e32 v116, v14
	v_mov_b32_e32 v117, v14
	v_mov_b32_e32 v118, v14
	v_mov_b32_e32 v119, v14
	v_mov_b32_e32 v120, v14
	v_mov_b32_e32 v121, v14
	v_mov_b32_e32 v2, v14
	v_mov_b32_e32 v3, v14
	v_mov_b32_e32 v4, v14
	v_mov_b32_e32 v5, v14
	v_mov_b32_e32 v6, v14
	v_mov_b32_e32 v7, v14
	v_mov_b32_e32 v8, v14
	v_mov_b32_e32 v9, v14
	v_mov_b32_e32 v34, v14
	v_mov_b32_e32 v35, v14
	v_mov_b32_e32 v36, v14
	v_mov_b32_e32 v37, v14
	v_mov_b32_e32 v38, v14
	v_mov_b32_e32 v39, v14
	v_mov_b32_e32 v40, v14
	v_mov_b32_e32 v41, v14
	v_mov_b32_e32 v66, v14
	v_mov_b32_e32 v67, v14
	v_mov_b32_e32 v68, v14
	v_mov_b32_e32 v69, v14
	v_mov_b32_e32 v70, v14
	v_mov_b32_e32 v71, v14
	v_mov_b32_e32 v72, v14
	v_mov_b32_e32 v73, v14
	v_mov_b32_e32 v98, v14
	v_mov_b32_e32 v99, v14
	v_mov_b32_e32 v100, v14
	v_mov_b32_e32 v101, v14
	v_mov_b32_e32 v102, v14
	v_mov_b32_e32 v103, v14
	v_mov_b32_e32 v104, v14
	v_mov_b32_e32 v105, v14
	v_mov_b32_e32 v10, v14
	v_mov_b32_e32 v11, v14
	v_mov_b32_e32 v12, v14
	v_mov_b32_e32 v13, v14
	v_mov_b32_e32 v18, v14
	v_mov_b32_e32 v19, v14
	v_mov_b32_e32 v20, v14
	v_mov_b32_e32 v21, v14
	v_mov_b32_e32 v42, v14
	v_mov_b32_e32 v43, v14
	v_mov_b32_e32 v44, v14
	v_mov_b32_e32 v45, v14
	v_mov_b32_e32 v54, v14
	v_mov_b32_e32 v55, v14
	v_mov_b32_e32 v56, v14
	v_mov_b32_e32 v57, v14
	v_mov_b32_e32 v82, v14
	v_mov_b32_e32 v83, v14
	v_mov_b32_e32 v84, v14
	v_mov_b32_e32 v85, v14
	v_mov_b32_e32 v94, v14
	v_mov_b32_e32 v95, v14
	v_mov_b32_e32 v96, v14
	v_mov_b32_e32 v97, v14
	v_mov_b32_e32 v122, v14
	v_mov_b32_e32 v123, v14
	v_mov_b32_e32 v124, v14
	v_mov_b32_e32 v125, v14
	v_mov_b32_e32 v126, v14
	v_mov_b32_e32 v127, v14
	v_mov_b32_e32 v128, v14
	v_mov_b32_e32 v129, v14
	.p2align 6
